# diff attention tile loop: LDS-DMA address arithmetic moved above the tile barrier (only the four DMA issues follow it)
# baseline (speedup 1.0000x reference)
; #define LAS __attribute__((address_space(3)))
; __device__ __forceinline__ void wait_tile(int younger) { if (younger >= 2) AT_WAIT(8); else if (younger == 1) AT_WAIT(4); else AT_WAIT(0); }
; #define AT_SCHED() __builtin_amdgcn_sched_barrier(0)
; template <int NDT>
; __device__ __forceinline__ void step64(LAS unsigned char* slot, const Addr<NDT>& a, const f16x8 (&qf)[4], f32x16 (&o)[NDT], float& m, float& l, f32x16& negm, bool& started) {
;     f16x8 kf[8], va[2 * NDT], vb[2 * NDT];
;     load_k<NDT>(slot, a, 0, kf); load_k<NDT>(slot, a, 8192, kf + 4);
;     load_v<NDT>(slot, a, 0, va);
;     AT_SCHED();
;     f32x16 s0 = qk32(kf, qf, negm), s1 = qk32(kf + 4, qf, negm);
;     AT_SCHED();
;     load_v<NDT>(slot, a, 8192, vb);
;     float mx = fmaxf(rowmax16(s0), rowmax16(s1)); mx = fmaxf(mx, __shfl_xor(mx, 32));
;     const float d = rescale<NDT>(mx, m, l, o, negm, started);
; __device__ __forceinline__ void diff_unit(int u, const f16* Z, f16* Y, const float* subln, float lam, LAS unsigned char* lds) {
;     ...
;     for (int t = 0; t < NT; ++t) {
;         wait_tile(NT - 1 - t);
;         __builtin_amdgcn_s_barrier();
;         if (t + 3 < NT) dma_tile(Z, DIFF_ROWBASE(t + 3), kcol, vcol, lds + ((t + 3) & 3) * SLOT, wave, lane);
;         step64<4>(lds + (t & 3) * SLOT, ad, qf, o, m, l, negm, started);
.LBB0_558:
	s_cmp_gt_u32 s18, 32
	s_cbranch_scc1 .Lmy_a0
	s_cmp_lt_u32 s18, 29
	s_cselect_b64 s[6:7], -1, 0
	s_add_i32 s3, s20, 0xfffff800
	s_and_b64 s[6:7], s[6:7], exec
	s_cselect_b32 s3, s20, s3
	s_cselect_b32 s6, s0, s16
	s_cselect_b32 s7, s1, s17
	s_add_u32 s6, s6, s3
	s_addc_u32 s7, s7, 0
	v_lshl_add_u64 v[4:5], s[6:7], 0, v[206:207]
	v_lshl_add_u64 v[8:9], s[6:7], 0, v[208:209]
	s_and_b32 s3, s19, 0x18000
	v_mad_u64_u32 v[6:7], s[8:9], v4, s71, v[204:205]
	s_add_i32 s21, s3, 0
	v_mad_i32_i24 v7, v5, s71, v7
	v_mad_u64_u32 v[10:11], s[8:9], v8, s71, v[204:205]
	v_mad_i32_i24 v11, v9, s71, v11
	s_lshl_b32 s86, s10, 1
	s_mov_b64 s[24:25], 0xc00
	v_lshl_add_u64 v[4:5], v[6:7], 0, s[86:87]
	v_lshl_add_u64 v[8:9], v[10:11], 0, s[86:87]
	s_mov_b32 s3, s87
	v_lshl_add_u64 v[4:5], v[4:5], 0, s[24:25]
	v_lshl_add_u64 v[8:9], v[8:9], 0, s[24:25]
	v_lshl_add_u64 v[6:7], v[6:7], 0, s[2:3]
	v_lshl_add_u64 v[10:11], v[10:11], 0, s[2:3]
	s_add_i32 s98, s13, s21
	s_add_i32 s22, s21, 0x4000
	s_add_i32 s99, s22, s13
	s_add_i32 s100, s14, s21
	s_add_i32 s101, s22, s14
	s_mov_b32 s8, m0
	s_barrier
	s_mov_b32 m0, s98
	s_nop 0
	global_load_lds_dwordx4 v[4:5], off
	s_mov_b32 m0, s99
	s_nop 0
	global_load_lds_dwordx4 v[6:7], off
	s_mov_b32 m0, s100
	s_nop 0
	global_load_lds_dwordx4 v[8:9], off
	s_mov_b32 m0, s101
	s_nop 0
	global_load_lds_dwordx4 v[10:11], off
	s_mov_b32 m0, s8
	s_branch .LBB0_560
.Lmy_a0:
	s_barrier
.LBB0_560:
	s_add_i32 s3, s19, 0xfffe8000
	s_and_b32 s3, s3, 0x18000
	s_add_i32 s3, s3, 0
	v_add_u32_e32 v2, s3, v219
	v_add_u32_e32 v4, s3, v221
	v_add_u32_e32 v5, s3, v220
	v_add_u32_e32 v6, s3, v222
	ds_read_b128 v[98:101], v2
	ds_read_b128 v[150:153], v2 offset:8192
	ds_read_b128 v[102:105], v4
	ds_read_b128 v[158:161], v4 offset:8192
	ds_read_b128 v[106:109], v5
	ds_read_b128 v[162:165], v5 offset:8192
	ds_read_b128 v[110:113], v6
	ds_read_b128 v[170:173], v6 offset:8192
	v_add_u32_e32 v2, s3, v223
	v_add_u32_e32 v16, s3, v224
	v_add_u32_e32 v17, s3, v225
	v_add_u32_e32 v186, s3, v226
	v_add_u32_e32 v190, s3, v227
	v_add_u32_e32 v191, s3, v228
	v_add_u32_e32 v233, s3, v229
	v_add_u32_e32 v192, s3, v230
	ds_read_b64_tr_b16 v[154:155], v2 offset:16384
	ds_read_b64_tr_b16 v[156:157], v16 offset:16384
	ds_read_b64_tr_b16 v[6:7], v16 offset:20480
	ds_read_b64_tr_b16 v[4:5], v2 offset:20480
	ds_read_b64_tr_b16 v[166:167], v17 offset:16384
	ds_read_b64_tr_b16 v[168:169], v186 offset:16384
	ds_read_b64_tr_b16 v[10:11], v186 offset:20480
	ds_read_b64_tr_b16 v[8:9], v17 offset:20480
	ds_read_b64_tr_b16 v[174:175], v190 offset:16384
	ds_read_b64_tr_b16 v[176:177], v191 offset:16384
	ds_read_b64_tr_b16 v[14:15], v191 offset:20480
	ds_read_b64_tr_b16 v[12:13], v190 offset:20480
	ds_read_b64_tr_b16 v[178:179], v233 offset:16384
	ds_read_b64_tr_b16 v[180:181], v192 offset:16384
	ds_read_b64_tr_b16 v[148:149], v192 offset:20480
	ds_read_b64_tr_b16 v[146:147], v233 offset:20480
	s_waitcnt lgkmcnt(14)
	v_mfma_f32_32x32x16_f16 v[114:129], v[98:101], v[142:145], v[82:97]
	v_mfma_f32_32x32x16_f16 v[114:129], v[102:105], v[138:141], v[114:129]
	v_mfma_f32_32x32x16_f16 v[114:129], v[106:109], v[134:137], v[114:129]
	v_mfma_f32_32x32x16_f16 v[114:129], v[110:113], v[130:133], v[114:129]
	v_mov_b64_e32 v[112:113], v[96:97]
	v_mov_b64_e32 v[110:111], v[94:95]
	v_mov_b64_e32 v[108:109], v[92:93]
	v_mov_b64_e32 v[106:107], v[90:91]
	v_mov_b64_e32 v[104:105], v[88:89]
	v_mov_b64_e32 v[102:103], v[86:87]
	v_mov_b64_e32 v[100:101], v[84:85]
	v_mov_b64_e32 v[98:99], v[82:83]
	s_nop 1
	v_mfma_f32_32x32x16_f16 v[98:113], v[150:153], v[142:145], v[98:113]
	v_mfma_f32_32x32x16_f16 v[98:113], v[158:161], v[138:141], v[98:113]
	v_mfma_f32_32x32x16_f16 v[98:113], v[162:165], v[134:137], v[98:113]
	v_mfma_f32_32x32x16_f16 v[98:113], v[170:173], v[130:133], v[98:113]
	ds_read_b64_tr_b16 v[170:171], v2 offset:24576
	ds_read_b64_tr_b16 v[172:173], v16 offset:24576
	ds_read_b64_tr_b16 v[152:153], v16 offset:28672
	ds_read_b64_tr_b16 v[150:151], v2 offset:28672
	ds_read_b64_tr_b16 v[182:183], v17 offset:24576
	ds_read_b64_tr_b16 v[184:185], v186 offset:24576
	ds_read_b64_tr_b16 v[160:161], v186 offset:28672
	ds_read_b64_tr_b16 v[158:159], v17 offset:28672
	ds_read_b64_tr_b16 v[186:187], v190 offset:24576
	ds_read_b64_tr_b16 v[188:189], v191 offset:24576
	ds_read_b64_tr_b16 v[164:165], v191 offset:28672
	ds_read_b64_tr_b16 v[162:163], v190 offset:28672
	v_max3_f32 v17, v98, v99, v100
	v_max3_f32 v190, v101, v102, v103
	v_max3_f32 v2, v114, v115, v116
	v_max3_f32 v16, v117, v118, v119
	s_nop 0
	v_max3_f32 v17, v17, v104, v105
	v_max3_f32 v190, v190, v106, v107
	v_max3_f32 v2, v2, v120, v121
	v_max3_f32 v16, v16, v122, v123
	s_nop 0
	v_max3_f32 v17, v17, v108, v109
	v_max3_f32 v190, v190, v110, v111
	v_max3_f32 v2, v2, v124, v125
	v_max3_f32 v16, v16, v126, v127
	s_nop 0
	v_max3_f32 v17, v17, v112, v113
	v_max_f32_e32 v190, v190, v190
	v_max_f32_e32 v17, v17, v17
	v_max3_f32 v2, v2, v128, v129
	v_max_f32_e32 v17, v17, v190
	v_max3_f32 v2, v2, v16, v17
	v_and_b32_e32 v17, 64, v215
	v_xor_b32_e32 v16, 32, v215
	v_add_u32_e32 v17, 64, v17
	v_cmp_lt_i32_e32 vcc, v16, v17
	ds_read_b64_tr_b16 v[194:195], v233 offset:24576
	ds_read_b64_tr_b16 v[196:197], v192 offset:24576
	ds_read_b64_tr_b16 v[192:193], v192 offset:28672
	ds_read_b64_tr_b16 v[190:191], v233 offset:28672
	v_cndmask_b32_e32 v16, v215, v16, vcc
	v_lshlrev_b32_e32 v217, 2, v16
	ds_bpermute_b32 v16, v217, v2
	s_waitcnt lgkmcnt(0)
	v_max_f32_e32 v16, v16, v16
	v_max_f32_e32 v17, v2, v16
	v_cmp_ge_f32_e32 vcc, s70, v17
	s_nop 1
	v_cndmask_b32_e64 v2, 0, 1, vcc
	v_cmp_eq_f32_e32 vcc, s72, v17
	s_nop 1
	v_cndmask_b32_e64 v16, 0, 1, vcc
	v_cndmask_b32_e64 v2, v16, v2, s[4:5]
	v_and_b32_e32 v2, 1, v2
	v_cmp_ne_u32_e32 vcc, 0, v2
	s_cmp_eq_u64 vcc, exec
	v_mov_b32_e32 v2, 0
	s_cbranch_scc1 .LBB0_568
	s_xor_b64 s[6:7], s[4:5], -1
	s_and_saveexec_b64 s[8:9], s[6:7]
	s_xor_b64 s[6:7], exec, s[8:9]
	s_cbranch_execz .LBB0_565
	v_cmp_lg_f32_e32 vcc, s72, v17
	s_mov_b64 s[4:5], 0
	v_mov_b32_e32 v2, 0
	s_and_saveexec_b64 s[8:9], vcc
	s_mov_b64 s[4:5], exec
	v_mov_b32_e32 v2, v17
	s_or_b64 exec, exec, s[8:9]

; __global__ void __launch_bounds__(512, 2) fwd(Params p) {
	.amdhsa_kernel _Z3fwd6Params
		.amdhsa_group_segment_fixed_size 0
		.amdhsa_private_segment_fixed_size 0
		.amdhsa_kernarg_size 576
		.amdhsa_user_sgpr_count 2
		.amdhsa_user_sgpr_dispatch_ptr 0
		.amdhsa_user_sgpr_queue_ptr 0
		.amdhsa_user_sgpr_kernarg_segment_ptr 1
		.amdhsa_user_sgpr_dispatch_id 0
		.amdhsa_user_sgpr_kernarg_preload_length 0
		.amdhsa_user_sgpr_kernarg_preload_offset 0
		.amdhsa_user_sgpr_private_segment_size 0
		.amdhsa_uses_dynamic_stack 0
		.amdhsa_enable_private_segment 0
		.amdhsa_system_sgpr_workgroup_id_x 1
		.amdhsa_system_sgpr_workgroup_id_y 0
		.amdhsa_system_sgpr_workgroup_id_z 0
		.amdhsa_system_sgpr_workgroup_info 0
		.amdhsa_system_vgpr_workitem_id 0
		.amdhsa_next_free_vgpr 252
		.amdhsa_next_free_sgpr 102
		.amdhsa_accum_offset 252
		.amdhsa_reserve_vcc 1
		.amdhsa_float_round_mode_32 0
		.amdhsa_float_round_mode_16_64 0
		.amdhsa_float_denorm_mode_32 3
		.amdhsa_float_denorm_mode_16_64 3
		.amdhsa_dx10_clamp 1
		.amdhsa_ieee_mode 1
		.amdhsa_fp16_overflow 0
		.amdhsa_tg_split 0
		.amdhsa_exception_fp_ieee_invalid_op 0
		.amdhsa_exception_fp_denorm_src 0
		.amdhsa_exception_fp_ieee_div_zero 0
		.amdhsa_exception_fp_ieee_overflow 0
		.amdhsa_exception_fp_ieee_underflow 0
		.amdhsa_exception_fp_ieee_inexact 0
		.amdhsa_exception_int_div_zero 0
	.end_amdhsa_kernel

; __global__ void __launch_bounds__(512, 2) fwd(Params p) {
amdhsa.kernels:
  - .agpr_count:     0
    .args:
      - .offset:         0
        .size:           320
        .value_kind:     by_value
      - .offset:         320
        .size:           4
        .value_kind:     hidden_block_count_x
      - .offset:         324
        .size:           4
        .value_kind:     hidden_block_count_y
      - .offset:         328
        .size:           4
        .value_kind:     hidden_block_count_z
      - .offset:         332
        .size:           2
        .value_kind:     hidden_group_size_x
      - .offset:         334
        .size:           2
        .value_kind:     hidden_group_size_y
      - .offset:         336
        .size:           2
        .value_kind:     hidden_group_size_z
      - .offset:         338
        .size:           2
        .value_kind:     hidden_remainder_x
      - .offset:         340
        .size:           2
        .value_kind:     hidden_remainder_y
      - .offset:         342
        .size:           2
        .value_kind:     hidden_remainder_z
      - .offset:         360
        .size:           8
        .value_kind:     hidden_global_offset_x
      - .offset:         368
        .size:           8
        .value_kind:     hidden_global_offset_y
      - .offset:         376
        .size:           8
        .value_kind:     hidden_global_offset_z
      - .offset:         384
        .size:           2
        .value_kind:     hidden_grid_dims
      - .offset:         440
        .size:           4
        .value_kind:     hidden_dynamic_lds_size
    .group_segment_fixed_size: 0
    .kernarg_segment_align: 8
    .kernarg_segment_size: 576
    .language:       OpenCL C
    .language_version:
      - 2
      - 0
    .max_flat_workgroup_size: 512
    .name:           _Z3fwd6Params
    .private_segment_fixed_size: 0
    .sgpr_count:     108
    .sgpr_spill_count: 133
    .symbol:         _Z3fwd6Params.kd
    .uniform_work_group_size: 1
    .uses_dynamic_stack: false
    .vgpr_count:     252
    .vgpr_spill_count: 0
    .wavefront_size: 64
